# speedup vs baseline: 1.0079x; 1.0022x over previous
.Lk4_st1_6:
	v_mfma_f32_16x16x32_f16 a[0:3], v[70:73], v[82:85], a[0:3]
	ds_read_b128 v[14:17], v144
	v_mfma_f32_16x16x32_f16 a[4:7], v[70:73], v[86:89], a[4:7]
	ds_read_b128 v[18:21], v146
	v_mfma_f32_16x16x32_f16 a[12:15], v[66:69], v[82:85], a[12:15]
	ds_read_b128 v[42:45], v166
	v_mfma_f32_16x16x32_f16 a[16:19], v[66:69], v[86:89], a[16:19]
	ds_read_b128 v[38:41], v166 offset:1024
	v_mfma_f32_16x16x32_f16 a[28:31], v[58:61], v[82:85], a[28:31]
	ds_read_b128 v[34:37], v166 offset:2048
	v_mfma_f32_16x16x32_f16 a[60:63], v[58:61], v[86:89], a[60:63]
	ds_read_b128 v[30:33], v166 offset:3072
	v_mfma_f32_16x16x32_f16 a[8:11], v[54:57], v[82:85], a[8:11]
	ds_read_b128 v[26:29], v166 offset:4096
	v_mfma_f32_16x16x32_f16 a[20:23], v[54:57], v[86:89], a[20:23]
	ds_read_b128 v[22:25], v166 offset:5120
	v_mfma_f32_16x16x32_f16 a[24:27], v[46:49], v[82:85], a[24:27]
	ds_read_b128 v[10:13], v166 offset:6144
	v_mfma_f32_16x16x32_f16 a[36:39], v[46:49], v[86:89], a[36:39]
	ds_read_b128 v[6:9], v166 offset:7168
	v_mfma_f32_16x16x32_f16 a[44:47], v[50:53], v[82:85], a[44:47]
	ds_read_b128 v[2:5], v166 offset:8192
	v_mfma_f32_16x16x32_f16 a[64:67], v[50:53], v[86:89], a[64:67]
	v_mfma_f32_16x16x32_f16 a[32:35], v[62:65], v[82:85], a[32:35]
	v_mfma_f32_16x16x32_f16 a[40:43], v[62:65], v[86:89], a[40:43]
	v_mfma_f32_16x16x32_f16 a[48:51], v[74:77], v[82:85], a[48:51]
	v_mfma_f32_16x16x32_f16 a[52:55], v[74:77], v[86:89], a[52:55]
	v_mfma_f32_16x16x32_f16 a[56:59], v[78:81], v[82:85], a[56:59]
	v_mfma_f32_16x16x32_f16 a[68:71], v[78:81], v[86:89], a[68:71]
	s_waitcnt lgkmcnt(8)
	v_mfma_f32_16x16x32_f16 a[0:3], v[42:45], v[14:17], a[0:3]
	ds_read_b128 v[82:85], v145
	v_mfma_f32_16x16x32_f16 a[4:7], v[42:45], v[18:21], a[4:7]
	ds_read_b128 v[86:89], v147
	s_waitcnt lgkmcnt(9)
	v_mfma_f32_16x16x32_f16 a[12:15], v[38:41], v[14:17], a[12:15]
	ds_read_b128 v[70:73], v166 offset:9216
	v_mfma_f32_16x16x32_f16 a[16:19], v[38:41], v[18:21], a[16:19]
	ds_read_b128 v[66:69], v166 offset:10240
	s_waitcnt lgkmcnt(10)
	v_mfma_f32_16x16x32_f16 a[28:31], v[34:37], v[14:17], a[28:31]
	ds_read_b128 v[58:61], v166 offset:11264
	v_mfma_f32_16x16x32_f16 a[60:63], v[34:37], v[18:21], a[60:63]
	ds_read_b128 v[54:57], v166 offset:12288
	s_waitcnt lgkmcnt(11)
	v_mfma_f32_16x16x32_f16 a[8:11], v[30:33], v[14:17], a[8:11]
	ds_read_b128 v[46:49], v166 offset:13312
	v_mfma_f32_16x16x32_f16 a[20:23], v[30:33], v[18:21], a[20:23]
	ds_read_b128 v[50:53], v166 offset:14336
	s_waitcnt lgkmcnt(12)
	v_mfma_f32_16x16x32_f16 a[24:27], v[26:29], v[14:17], a[24:27]
	ds_read_b128 v[62:65], v166 offset:15360
	v_mfma_f32_16x16x32_f16 a[36:39], v[26:29], v[18:21], a[36:39]
	ds_read_b128 v[74:77], v166 offset:16384
	s_waitcnt lgkmcnt(13)
	v_mfma_f32_16x16x32_f16 a[44:47], v[22:25], v[14:17], a[44:47]
	ds_read_b128 v[78:81], v166 offset:17408
	v_mfma_f32_16x16x32_f16 a[64:67], v[22:25], v[18:21], a[64:67]
	s_waitcnt lgkmcnt(13)
	v_mfma_f32_16x16x32_f16 a[32:35], v[10:13], v[14:17], a[32:35]
	v_mfma_f32_16x16x32_f16 a[40:43], v[10:13], v[18:21], a[40:43]
	s_waitcnt lgkmcnt(12)
	v_mfma_f32_16x16x32_f16 a[48:51], v[6:9], v[14:17], a[48:51]
	v_mfma_f32_16x16x32_f16 a[52:55], v[6:9], v[18:21], a[52:55]
	s_waitcnt lgkmcnt(11)
	v_mfma_f32_16x16x32_f16 a[56:59], v[2:5], v[14:17], a[56:59]
	v_mfma_f32_16x16x32_f16 a[68:71], v[2:5], v[18:21], a[68:71]
	s_waitcnt lgkmcnt(8)
	v_mfma_f32_16x16x32_f16 a[0:3], v[70:73], v[82:85], a[0:3]
	ds_read_b128 v[14:17], v148
	v_mfma_f32_16x16x32_f16 a[4:7], v[70:73], v[86:89], a[4:7]
	ds_read_b128 v[18:21], v150
	s_waitcnt lgkmcnt(9)
	v_mfma_f32_16x16x32_f16 a[12:15], v[66:69], v[82:85], a[12:15]
	ds_read_b128 v[42:45], v167
	v_mfma_f32_16x16x32_f16 a[16:19], v[66:69], v[86:89], a[16:19]
	ds_read_b128 v[38:41], v167 offset:1024
	s_waitcnt lgkmcnt(10)
	v_mfma_f32_16x16x32_f16 a[28:31], v[58:61], v[82:85], a[28:31]
	ds_read_b128 v[34:37], v167 offset:2048
	v_mfma_f32_16x16x32_f16 a[60:63], v[58:61], v[86:89], a[60:63]
	ds_read_b128 v[30:33], v167 offset:3072
	s_waitcnt lgkmcnt(11)
	v_mfma_f32_16x16x32_f16 a[8:11], v[54:57], v[82:85], a[8:11]
	ds_read_b128 v[26:29], v167 offset:4096
	v_mfma_f32_16x16x32_f16 a[20:23], v[54:57], v[86:89], a[20:23]
	ds_read_b128 v[22:25], v167 offset:5120
	s_waitcnt lgkmcnt(12)
	v_mfma_f32_16x16x32_f16 a[24:27], v[46:49], v[82:85], a[24:27]
	ds_read_b128 v[10:13], v167 offset:6144
	v_mfma_f32_16x16x32_f16 a[36:39], v[46:49], v[86:89], a[36:39]
	ds_read_b128 v[6:9], v167 offset:7168
	s_waitcnt lgkmcnt(13)
	v_mfma_f32_16x16x32_f16 a[44:47], v[50:53], v[82:85], a[44:47]
	ds_read_b128 v[2:5], v167 offset:8192
	v_mfma_f32_16x16x32_f16 a[64:67], v[50:53], v[86:89], a[64:67]
	s_waitcnt lgkmcnt(13)
	v_mfma_f32_16x16x32_f16 a[32:35], v[62:65], v[82:85], a[32:35]
	v_mfma_f32_16x16x32_f16 a[40:43], v[62:65], v[86:89], a[40:43]
	s_waitcnt lgkmcnt(12)
	v_mfma_f32_16x16x32_f16 a[48:51], v[74:77], v[82:85], a[48:51]
	v_mfma_f32_16x16x32_f16 a[52:55], v[74:77], v[86:89], a[52:55]
	s_waitcnt lgkmcnt(11)
	v_mfma_f32_16x16x32_f16 a[56:59], v[78:81], v[82:85], a[56:59]
	v_mfma_f32_16x16x32_f16 a[68:71], v[78:81], v[86:89], a[68:71]
	s_waitcnt lgkmcnt(8)
	v_mfma_f32_16x16x32_f16 a[0:3], v[42:45], v[14:17], a[0:3]
	ds_read_b128 v[82:85], v149
	v_mfma_f32_16x16x32_f16 a[4:7], v[42:45], v[18:21], a[4:7]
	ds_read_b128 v[86:89], v151
	s_waitcnt lgkmcnt(9)
	v_mfma_f32_16x16x32_f16 a[12:15], v[38:41], v[14:17], a[12:15]
	ds_read_b128 v[70:73], v167 offset:9216
	v_mfma_f32_16x16x32_f16 a[16:19], v[38:41], v[18:21], a[16:19]
	ds_read_b128 v[66:69], v167 offset:10240
	s_waitcnt lgkmcnt(10)
	v_mfma_f32_16x16x32_f16 a[28:31], v[34:37], v[14:17], a[28:31]
	ds_read_b128 v[58:61], v167 offset:11264
	v_mfma_f32_16x16x32_f16 a[60:63], v[34:37], v[18:21], a[60:63]
	ds_read_b128 v[54:57], v167 offset:12288
	s_waitcnt lgkmcnt(11)
	v_mfma_f32_16x16x32_f16 a[8:11], v[30:33], v[14:17], a[8:11]
	ds_read_b128 v[46:49], v167 offset:13312
	v_mfma_f32_16x16x32_f16 a[20:23], v[30:33], v[18:21], a[20:23]
	ds_read_b128 v[50:53], v167 offset:14336
	s_waitcnt lgkmcnt(12)
	v_mfma_f32_16x16x32_f16 a[24:27], v[26:29], v[14:17], a[24:27]
	ds_read_b128 v[62:65], v167 offset:15360
	v_mfma_f32_16x16x32_f16 a[36:39], v[26:29], v[18:21], a[36:39]
	ds_read_b128 v[74:77], v167 offset:16384
	s_waitcnt lgkmcnt(13)
	v_mfma_f32_16x16x32_f16 a[44:47], v[22:25], v[14:17], a[44:47]
	ds_read_b128 v[78:81], v167 offset:17408
	v_mfma_f32_16x16x32_f16 a[64:67], v[22:25], v[18:21], a[64:67]
	s_waitcnt lgkmcnt(13)
	v_mfma_f32_16x16x32_f16 a[32:35], v[10:13], v[14:17], a[32:35]
	v_mfma_f32_16x16x32_f16 a[40:43], v[10:13], v[18:21], a[40:43]
	s_waitcnt lgkmcnt(12)
	v_mfma_f32_16x16x32_f16 a[48:51], v[6:9], v[14:17], a[48:51]
	v_mfma_f32_16x16x32_f16 a[52:55], v[6:9], v[18:21], a[52:55]
	s_waitcnt lgkmcnt(11)
	v_mfma_f32_16x16x32_f16 a[56:59], v[2:5], v[14:17], a[56:59]
	v_mfma_f32_16x16x32_f16 a[68:71], v[2:5], v[18:21], a[68:71]
	s_waitcnt lgkmcnt(8)
	v_mfma_f32_16x16x32_f16 a[0:3], v[70:73], v[82:85], a[0:3]
	ds_read_b128 v[14:17], v150
	v_mfma_f32_16x16x32_f16 a[4:7], v[70:73], v[86:89], a[4:7]
	ds_read_b128 v[18:21], v152
	s_waitcnt lgkmcnt(9)
	v_mfma_f32_16x16x32_f16 a[12:15], v[66:69], v[82:85], a[12:15]
	ds_read_b128 v[42:45], v168
	v_mfma_f32_16x16x32_f16 a[16:19], v[66:69], v[86:89], a[16:19]
	ds_read_b128 v[38:41], v168 offset:1024
	s_waitcnt lgkmcnt(10)
	v_mfma_f32_16x16x32_f16 a[28:31], v[58:61], v[82:85], a[28:31]
	ds_read_b128 v[34:37], v168 offset:2048
	v_mfma_f32_16x16x32_f16 a[60:63], v[58:61], v[86:89], a[60:63]
	ds_read_b128 v[30:33], v168 offset:3072
	s_waitcnt lgkmcnt(11)
	v_mfma_f32_16x16x32_f16 a[8:11], v[54:57], v[82:85], a[8:11]
	ds_read_b128 v[26:29], v168 offset:4096
	v_mfma_f32_16x16x32_f16 a[20:23], v[54:57], v[86:89], a[20:23]
	ds_read_b128 v[22:25], v168 offset:5120
	s_waitcnt lgkmcnt(12)
	v_mfma_f32_16x16x32_f16 a[24:27], v[46:49], v[82:85], a[24:27]
	ds_read_b128 v[10:13], v168 offset:6144
	v_mfma_f32_16x16x32_f16 a[36:39], v[46:49], v[86:89], a[36:39]
	ds_read_b128 v[6:9], v168 offset:7168
	s_waitcnt lgkmcnt(13)
	v_mfma_f32_16x16x32_f16 a[44:47], v[50:53], v[82:85], a[44:47]
	ds_read_b128 v[2:5], v168 offset:8192
	v_mfma_f32_16x16x32_f16 a[64:67], v[50:53], v[86:89], a[64:67]
	s_waitcnt lgkmcnt(13)
	v_mfma_f32_16x16x32_f16 a[32:35], v[62:65], v[82:85], a[32:35]
	v_mfma_f32_16x16x32_f16 a[40:43], v[62:65], v[86:89], a[40:43]
	s_waitcnt lgkmcnt(12)
	v_mfma_f32_16x16x32_f16 a[48:51], v[74:77], v[82:85], a[48:51]
	v_mfma_f32_16x16x32_f16 a[52:55], v[74:77], v[86:89], a[52:55]
	s_waitcnt lgkmcnt(11)
	v_mfma_f32_16x16x32_f16 a[56:59], v[78:81], v[82:85], a[56:59]
	v_mfma_f32_16x16x32_f16 a[68:71], v[78:81], v[86:89], a[68:71]
	s_waitcnt lgkmcnt(8)
	v_mfma_f32_16x16x32_f16 a[0:3], v[42:45], v[14:17], a[0:3]
	ds_read_b128 v[82:85], v151
	v_mfma_f32_16x16x32_f16 a[4:7], v[42:45], v[18:21], a[4:7]
	ds_read_b128 v[86:89], v153
	s_waitcnt lgkmcnt(9)
	v_mfma_f32_16x16x32_f16 a[12:15], v[38:41], v[14:17], a[12:15]
	ds_read_b128 v[70:73], v168 offset:9216
	v_mfma_f32_16x16x32_f16 a[16:19], v[38:41], v[18:21], a[16:19]
	ds_read_b128 v[66:69], v168 offset:10240
	s_waitcnt lgkmcnt(10)
	v_mfma_f32_16x16x32_f16 a[28:31], v[34:37], v[14:17], a[28:31]
	ds_read_b128 v[58:61], v168 offset:11264
	v_mfma_f32_16x16x32_f16 a[60:63], v[34:37], v[18:21], a[60:63]
	ds_read_b128 v[54:57], v168 offset:12288
	s_waitcnt lgkmcnt(11)
	v_mfma_f32_16x16x32_f16 a[8:11], v[30:33], v[14:17], a[8:11]
	ds_read_b128 v[46:49], v168 offset:13312
	v_mfma_f32_16x16x32_f16 a[20:23], v[30:33], v[18:21], a[20:23]
	ds_read_b128 v[50:53], v168 offset:14336
	s_waitcnt lgkmcnt(12)
	v_mfma_f32_16x16x32_f16 a[24:27], v[26:29], v[14:17], a[24:27]
	ds_read_b128 v[62:65], v168 offset:15360
	v_mfma_f32_16x16x32_f16 a[36:39], v[26:29], v[18:21], a[36:39]
	ds_read_b128 v[74:77], v168 offset:16384
	s_waitcnt lgkmcnt(13)
	v_mfma_f32_16x16x32_f16 a[44:47], v[22:25], v[14:17], a[44:47]
	ds_read_b128 v[78:81], v168 offset:17408
	v_mfma_f32_16x16x32_f16 a[64:67], v[22:25], v[18:21], a[64:67]
	s_waitcnt lgkmcnt(13)
	v_mfma_f32_16x16x32_f16 a[32:35], v[10:13], v[14:17], a[32:35]
	v_mfma_f32_16x16x32_f16 a[40:43], v[10:13], v[18:21], a[40:43]
	s_waitcnt lgkmcnt(12)
	v_mfma_f32_16x16x32_f16 a[48:51], v[6:9], v[14:17], a[48:51]
	v_mfma_f32_16x16x32_f16 a[52:55], v[6:9], v[18:21], a[52:55]
	s_waitcnt lgkmcnt(11)
	v_mfma_f32_16x16x32_f16 a[56:59], v[2:5], v[14:17], a[56:59]
	v_mfma_f32_16x16x32_f16 a[68:71], v[2:5], v[18:21], a[68:71]
	s_waitcnt vmcnt(0) lgkmcnt(0)
	s_barrier
	s_add_u32 s52, s50, 0x1f800
	s_addc_u32 s53, s51, 0
	s_add_i32 m0, s42, 0x1f000
	s_nop 0
	global_load_lds_dwordx4 v137, s[52:53]
	s_add_i32 m0, s43, 0x1f000
	s_nop 0
	global_load_lds_dwordx4 v138, s[52:53]
	s_cmp_lt_u32 s42, 0x800
	s_cbranch_scc0 .Lk4_st4_7
	s_add_i32 m0, s44, 0x1f000
	s_nop 0
	global_load_lds_dwordx4 v139, s[52:53]
.Lk4_st4_7:
	v_add_u32_e32 v128, s17, v118
	s_nop 1
	v_readfirstlane_b32 s14, v128
	s_mov_b32 m0, s14
	s_nop 0
	global_load_lds_dwordx4 v[102:103], off nt
	v_add_u32_e32 v128, s17, v90
	s_nop 1
	v_readfirstlane_b32 s14, v128
	s_mov_b32 m0, s14
	s_nop 0
	global_load_lds_dwordx4 v[104:105], off nt
	v_add_u32_e32 v128, s17, v91
	s_nop 1
	v_readfirstlane_b32 s14, v128
	s_mov_b32 m0, s14
	s_nop 0
	global_load_lds_dwordx4 v[108:109], off nt
	v_add_u32_e32 v128, s17, v119
	s_nop 1
	v_readfirstlane_b32 s14, v128
	s_mov_b32 m0, s14
	s_nop 0
	global_load_lds_dwordx4 v[112:113], off nt
	v_mfma_f32_16x16x32_f16 a[0:3], v[70:73], v[82:85], a[0:3]
	ds_read_b128 v[14:17], v152
	v_mfma_f32_16x16x32_f16 a[4:7], v[70:73], v[86:89], a[4:7]
	ds_read_b128 v[18:21], v154
	v_mfma_f32_16x16x32_f16 a[12:15], v[66:69], v[82:85], a[12:15]
	ds_read_b128 v[42:45], v164
	v_mfma_f32_16x16x32_f16 a[16:19], v[66:69], v[86:89], a[16:19]
	ds_read_b128 v[38:41], v164 offset:1024
	v_mfma_f32_16x16x32_f16 a[28:31], v[58:61], v[82:85], a[28:31]
	ds_read_b128 v[34:37], v164 offset:2048
	v_mfma_f32_16x16x32_f16 a[60:63], v[58:61], v[86:89], a[60:63]
	ds_read_b128 v[30:33], v164 offset:3072
	v_mfma_f32_16x16x32_f16 a[8:11], v[54:57], v[82:85], a[8:11]
	ds_read_b128 v[26:29], v164 offset:4096
	v_mfma_f32_16x16x32_f16 a[20:23], v[54:57], v[86:89], a[20:23]
	ds_read_b128 v[22:25], v164 offset:5120
	v_mfma_f32_16x16x32_f16 a[24:27], v[46:49], v[82:85], a[24:27]
	ds_read_b128 v[10:13], v164 offset:6144
	v_mfma_f32_16x16x32_f16 a[36:39], v[46:49], v[86:89], a[36:39]
	ds_read_b128 v[6:9], v164 offset:7168
	v_mfma_f32_16x16x32_f16 a[44:47], v[50:53], v[82:85], a[44:47]
	ds_read_b128 v[2:5], v164 offset:8192
	v_mfma_f32_16x16x32_f16 a[64:67], v[50:53], v[86:89], a[64:67]
	v_mfma_f32_16x16x32_f16 a[32:35], v[62:65], v[82:85], a[32:35]
	v_mfma_f32_16x16x32_f16 a[40:43], v[62:65], v[86:89], a[40:43]
	v_mfma_f32_16x16x32_f16 a[48:51], v[74:77], v[82:85], a[48:51]
	v_mfma_f32_16x16x32_f16 a[52:55], v[74:77], v[86:89], a[52:55]
	v_mfma_f32_16x16x32_f16 a[56:59], v[78:81], v[82:85], a[56:59]
	v_mfma_f32_16x16x32_f16 a[68:71], v[78:81], v[86:89], a[68:71]
	s_waitcnt lgkmcnt(8)
	v_mfma_f32_16x16x32_f16 a[0:3], v[42:45], v[14:17], a[0:3]
	ds_read_b128 v[82:85], v153
	v_mfma_f32_16x16x32_f16 a[4:7], v[42:45], v[18:21], a[4:7]
	ds_read_b128 v[86:89], v155
	s_waitcnt lgkmcnt(9)
	v_mfma_f32_16x16x32_f16 a[12:15], v[38:41], v[14:17], a[12:15]
	ds_read_b128 v[70:73], v164 offset:9216
	v_mfma_f32_16x16x32_f16 a[16:19], v[38:41], v[18:21], a[16:19]
	ds_read_b128 v[66:69], v164 offset:10240
	s_waitcnt lgkmcnt(10)
	v_mfma_f32_16x16x32_f16 a[28:31], v[34:37], v[14:17], a[28:31]
	ds_read_b128 v[58:61], v164 offset:11264
	v_mfma_f32_16x16x32_f16 a[60:63], v[34:37], v[18:21], a[60:63]
	ds_read_b128 v[54:57], v164 offset:12288
	s_waitcnt lgkmcnt(11)
	v_mfma_f32_16x16x32_f16 a[8:11], v[30:33], v[14:17], a[8:11]
	ds_read_b128 v[46:49], v164 offset:13312
	v_mfma_f32_16x16x32_f16 a[20:23], v[30:33], v[18:21], a[20:23]
	ds_read_b128 v[50:53], v164 offset:14336
	s_waitcnt lgkmcnt(12)
	v_mfma_f32_16x16x32_f16 a[24:27], v[26:29], v[14:17], a[24:27]
	ds_read_b128 v[62:65], v164 offset:15360
	v_mfma_f32_16x16x32_f16 a[36:39], v[26:29], v[18:21], a[36:39]
	ds_read_b128 v[74:77], v164 offset:16384
	s_waitcnt lgkmcnt(13)
	v_mfma_f32_16x16x32_f16 a[44:47], v[22:25], v[14:17], a[44:47]
	ds_read_b128 v[78:81], v164 offset:17408
	v_mfma_f32_16x16x32_f16 a[64:67], v[22:25], v[18:21], a[64:67]
	s_waitcnt lgkmcnt(13)
	v_mfma_f32_16x16x32_f16 a[32:35], v[10:13], v[14:17], a[32:35]
	v_mfma_f32_16x16x32_f16 a[40:43], v[10:13], v[18:21], a[40:43]
	s_waitcnt lgkmcnt(12)
	v_mfma_f32_16x16x32_f16 a[48:51], v[6:9], v[14:17], a[48:51]
	v_mfma_f32_16x16x32_f16 a[52:55], v[6:9], v[18:21], a[52:55]
	s_waitcnt lgkmcnt(11)
	v_mfma_f32_16x16x32_f16 a[56:59], v[2:5], v[14:17], a[56:59]
	v_mfma_f32_16x16x32_f16 a[68:71], v[2:5], v[18:21], a[68:71]
	s_waitcnt lgkmcnt(8)
	v_mfma_f32_16x16x32_f16 a[0:3], v[70:73], v[82:85], a[0:3]
	ds_read_b128 v[14:17], v156
	v_mfma_f32_16x16x32_f16 a[4:7], v[70:73], v[86:89], a[4:7]
	ds_read_b128 v[18:21], v158
	s_waitcnt lgkmcnt(9)
	v_mfma_f32_16x16x32_f16 a[12:15], v[66:69], v[82:85], a[12:15]
	ds_read_b128 v[42:45], v165
	v_mfma_f32_16x16x32_f16 a[16:19], v[66:69], v[86:89], a[16:19]
	ds_read_b128 v[38:41], v165 offset:1024
	s_waitcnt lgkmcnt(10)
	v_mfma_f32_16x16x32_f16 a[28:31], v[58:61], v[82:85], a[28:31]
	ds_read_b128 v[34:37], v165 offset:2048
	v_mfma_f32_16x16x32_f16 a[60:63], v[58:61], v[86:89], a[60:63]
	ds_read_b128 v[30:33], v165 offset:3072
	s_waitcnt lgkmcnt(11)
	v_mfma_f32_16x16x32_f16 a[8:11], v[54:57], v[82:85], a[8:11]
	ds_read_b128 v[26:29], v165 offset:4096
	v_mfma_f32_16x16x32_f16 a[20:23], v[54:57], v[86:89], a[20:23]
	ds_read_b128 v[22:25], v165 offset:5120
	s_waitcnt lgkmcnt(12)
	v_mfma_f32_16x16x32_f16 a[24:27], v[46:49], v[82:85], a[24:27]
	ds_read_b128 v[10:13], v165 offset:6144
	v_mfma_f32_16x16x32_f16 a[36:39], v[46:49], v[86:89], a[36:39]
	ds_read_b128 v[6:9], v165 offset:7168
	s_waitcnt lgkmcnt(13)
	v_mfma_f32_16x16x32_f16 a[44:47], v[50:53], v[82:85], a[44:47]
	ds_read_b128 v[2:5], v165 offset:8192
	v_mfma_f32_16x16x32_f16 a[64:67], v[50:53], v[86:89], a[64:67]
	s_waitcnt lgkmcnt(13)
	v_mfma_f32_16x16x32_f16 a[32:35], v[62:65], v[82:85], a[32:35]
	v_mfma_f32_16x16x32_f16 a[40:43], v[62:65], v[86:89], a[40:43]
	s_waitcnt lgkmcnt(12)
	v_mfma_f32_16x16x32_f16 a[48:51], v[74:77], v[82:85], a[48:51]
	v_mfma_f32_16x16x32_f16 a[52:55], v[74:77], v[86:89], a[52:55]
	s_waitcnt lgkmcnt(11)
	v_mfma_f32_16x16x32_f16 a[56:59], v[78:81], v[82:85], a[56:59]
	v_mfma_f32_16x16x32_f16 a[68:71], v[78:81], v[86:89], a[68:71]
	s_waitcnt lgkmcnt(8)
	v_mfma_f32_16x16x32_f16 a[0:3], v[42:45], v[14:17], a[0:3]
	ds_read_b128 v[82:85], v157
	v_mfma_f32_16x16x32_f16 a[4:7], v[42:45], v[18:21], a[4:7]
	ds_read_b128 v[86:89], v159
	s_waitcnt lgkmcnt(9)
	v_mfma_f32_16x16x32_f16 a[12:15], v[38:41], v[14:17], a[12:15]
	ds_read_b128 v[70:73], v165 offset:9216
	v_mfma_f32_16x16x32_f16 a[16:19], v[38:41], v[18:21], a[16:19]
	ds_read_b128 v[66:69], v165 offset:10240
	s_waitcnt lgkmcnt(10)
	v_mfma_f32_16x16x32_f16 a[28:31], v[34:37], v[14:17], a[28:31]
	ds_read_b128 v[58:61], v165 offset:11264
	v_mfma_f32_16x16x32_f16 a[60:63], v[34:37], v[18:21], a[60:63]
	ds_read_b128 v[54:57], v165 offset:12288
	s_waitcnt lgkmcnt(11)
	v_mfma_f32_16x16x32_f16 a[8:11], v[30:33], v[14:17], a[8:11]
	ds_read_b128 v[46:49], v165 offset:13312
	v_mfma_f32_16x16x32_f16 a[20:23], v[30:33], v[18:21], a[20:23]
	ds_read_b128 v[50:53], v165 offset:14336
	s_waitcnt lgkmcnt(12)
	v_mfma_f32_16x16x32_f16 a[24:27], v[26:29], v[14:17], a[24:27]
	ds_read_b128 v[62:65], v165 offset:15360
	v_mfma_f32_16x16x32_f16 a[36:39], v[26:29], v[18:21], a[36:39]
	ds_read_b128 v[74:77], v165 offset:16384
	s_waitcnt lgkmcnt(13)
	v_mfma_f32_16x16x32_f16 a[44:47], v[22:25], v[14:17], a[44:47]
	ds_read_b128 v[78:81], v165 offset:17408
	v_mfma_f32_16x16x32_f16 a[64:67], v[22:25], v[18:21], a[64:67]
	s_waitcnt lgkmcnt(13)
	v_mfma_f32_16x16x32_f16 a[32:35], v[10:13], v[14:17], a[32:35]
	v_mfma_f32_16x16x32_f16 a[40:43], v[10:13], v[18:21], a[40:43]
	s_waitcnt lgkmcnt(12)
	v_mfma_f32_16x16x32_f16 a[48:51], v[6:9], v[14:17], a[48:51]
	v_mfma_f32_16x16x32_f16 a[52:55], v[6:9], v[18:21], a[52:55]
	s_waitcnt lgkmcnt(11)
	v_mfma_f32_16x16x32_f16 a[56:59], v[2:5], v[14:17], a[56:59]
	v_mfma_f32_16x16x32_f16 a[68:71], v[2:5], v[18:21], a[68:71]
	s_waitcnt vmcnt(4) lgkmcnt(0)
	s_barrier
	s_add_u32 s52, s50, 0x24000
	s_addc_u32 s53, s51, 0
	s_add_i32 m0, s42, 0xc600
	s_nop 0
	global_load_lds_dwordx4 v137, s[52:53]
	s_add_i32 m0, s43, 0xc600
	s_nop 0
	global_load_lds_dwordx4 v138, s[52:53]
	s_cmp_lt_u32 s42, 0x800
	s_cbranch_scc0 .Lk4_st6_8
	s_add_i32 m0, s44, 0xc600
	s_nop 0
	global_load_lds_dwordx4 v139, s[52:53]
.Lk4_st6_8:
	v_mfma_f32_16x16x32_f16 a[0:3], v[70:73], v[82:85], a[0:3]
	ds_read_b128 v[14:17], v158
	v_mfma_f32_16x16x32_f16 a[4:7], v[70:73], v[86:89], a[4:7]
	ds_read_b128 v[18:21], v160
	v_mfma_f32_16x16x32_f16 a[12:15], v[66:69], v[82:85], a[12:15]
	ds_read_b128 v[42:45], v168
	v_mfma_f32_16x16x32_f16 a[16:19], v[66:69], v[86:89], a[16:19]
	ds_read_b128 v[38:41], v168 offset:1024
	v_mfma_f32_16x16x32_f16 a[28:31], v[58:61], v[82:85], a[28:31]
	ds_read_b128 v[34:37], v168 offset:2048
	v_mfma_f32_16x16x32_f16 a[60:63], v[58:61], v[86:89], a[60:63]
	ds_read_b128 v[30:33], v168 offset:3072
	v_mfma_f32_16x16x32_f16 a[8:11], v[54:57], v[82:85], a[8:11]
	ds_read_b128 v[26:29], v168 offset:4096
	v_mfma_f32_16x16x32_f16 a[20:23], v[54:57], v[86:89], a[20:23]
	ds_read_b128 v[22:25], v168 offset:5120
	v_mfma_f32_16x16x32_f16 a[24:27], v[46:49], v[82:85], a[24:27]
	ds_read_b128 v[10:13], v168 offset:6144
	v_mfma_f32_16x16x32_f16 a[36:39], v[46:49], v[86:89], a[36:39]
	ds_read_b128 v[6:9], v168 offset:7168
	v_mfma_f32_16x16x32_f16 a[44:47], v[50:53], v[82:85], a[44:47]
	ds_read_b128 v[2:5], v168 offset:8192
	v_mfma_f32_16x16x32_f16 a[64:67], v[50:53], v[86:89], a[64:67]
	v_mfma_f32_16x16x32_f16 a[32:35], v[62:65], v[82:85], a[32:35]
	v_mfma_f32_16x16x32_f16 a[40:43], v[62:65], v[86:89], a[40:43]
	v_mfma_f32_16x16x32_f16 a[48:51], v[74:77], v[82:85], a[48:51]
	v_mfma_f32_16x16x32_f16 a[52:55], v[74:77], v[86:89], a[52:55]
	v_mfma_f32_16x16x32_f16 a[56:59], v[78:81], v[82:85], a[56:59]
	v_mfma_f32_16x16x32_f16 a[68:71], v[78:81], v[86:89], a[68:71]
	s_waitcnt lgkmcnt(8)
	v_mfma_f32_16x16x32_f16 a[0:3], v[42:45], v[14:17], a[0:3]
	ds_read_b128 v[82:85], v159
	v_mfma_f32_16x16x32_f16 a[4:7], v[42:45], v[18:21], a[4:7]
	ds_read_b128 v[86:89], v161
	s_waitcnt lgkmcnt(9)
	v_mfma_f32_16x16x32_f16 a[12:15], v[38:41], v[14:17], a[12:15]
	ds_read_b128 v[70:73], v168 offset:9216
	v_mfma_f32_16x16x32_f16 a[16:19], v[38:41], v[18:21], a[16:19]
	ds_read_b128 v[66:69], v168 offset:10240
	s_waitcnt lgkmcnt(10)
	v_mfma_f32_16x16x32_f16 a[28:31], v[34:37], v[14:17], a[28:31]
	ds_read_b128 v[58:61], v168 offset:11264
	v_mfma_f32_16x16x32_f16 a[60:63], v[34:37], v[18:21], a[60:63]
	ds_read_b128 v[54:57], v168 offset:12288
	s_waitcnt lgkmcnt(11)
	v_mfma_f32_16x16x32_f16 a[8:11], v[30:33], v[14:17], a[8:11]
	ds_read_b128 v[46:49], v168 offset:13312
	v_mfma_f32_16x16x32_f16 a[20:23], v[30:33], v[18:21], a[20:23]
	ds_read_b128 v[50:53], v168 offset:14336
	s_waitcnt lgkmcnt(12)
	v_mfma_f32_16x16x32_f16 a[24:27], v[26:29], v[14:17], a[24:27]
	ds_read_b128 v[62:65], v168 offset:15360
	v_mfma_f32_16x16x32_f16 a[36:39], v[26:29], v[18:21], a[36:39]
	ds_read_b128 v[74:77], v168 offset:16384
	s_waitcnt lgkmcnt(13)
	v_mfma_f32_16x16x32_f16 a[44:47], v[22:25], v[14:17], a[44:47]
	ds_read_b128 v[78:81], v168 offset:17408
	v_mfma_f32_16x16x32_f16 a[64:67], v[22:25], v[18:21], a[64:67]
	s_waitcnt lgkmcnt(13)
	v_mfma_f32_16x16x32_f16 a[32:35], v[10:13], v[14:17], a[32:35]
	v_mfma_f32_16x16x32_f16 a[40:43], v[10:13], v[18:21], a[40:43]
	s_waitcnt lgkmcnt(12)
	v_mfma_f32_16x16x32_f16 a[48:51], v[6:9], v[14:17], a[48:51]
	v_mfma_f32_16x16x32_f16 a[52:55], v[6:9], v[18:21], a[52:55]
	s_waitcnt lgkmcnt(11)
	v_mfma_f32_16x16x32_f16 a[56:59], v[2:5], v[14:17], a[56:59]
	v_mfma_f32_16x16x32_f16 a[68:71], v[2:5], v[18:21], a[68:71]
	s_waitcnt vmcnt(0) lgkmcnt(0)
	s_barrier
	v_add_u32_e32 v128, s16, v118
	s_nop 1
	v_readfirstlane_b32 s14, v128
	s_mov_b32 m0, s14
	s_nop 0
	global_load_lds_dwordx4 v[0:1], off nt
	v_add_u32_e32 v128, s16, v90
	s_nop 1
	v_readfirstlane_b32 s14, v128
	s_mov_b32 m0, s14
	s_nop 0
	global_load_lds_dwordx4 v[106:107], off nt
	v_add_u32_e32 v128, s16, v91
	s_nop 1
	v_readfirstlane_b32 s14, v128
	s_mov_b32 m0, s14
	s_nop 0
	global_load_lds_dwordx4 v[110:111], off nt
	v_add_u32_e32 v128, s16, v119
	s_nop 1
	v_readfirstlane_b32 s14, v128
	s_mov_b32 m0, s14
	s_nop 0
	global_load_lds_dwordx4 v[114:115], off nt
	v_mfma_f32_16x16x32_f16 a[0:3], v[70:73], v[82:85], a[0:3]
	ds_read_b128 v[14:17], v160
	v_mfma_f32_16x16x32_f16 a[4:7], v[70:73], v[86:89], a[4:7]
	ds_read_b128 v[18:21], v162
	v_mfma_f32_16x16x32_f16 a[12:15], v[66:69], v[82:85], a[12:15]
	ds_read_b128 v[42:45], v164
	v_mfma_f32_16x16x32_f16 a[16:19], v[66:69], v[86:89], a[16:19]
	ds_read_b128 v[38:41], v164 offset:1024
	v_mfma_f32_16x16x32_f16 a[28:31], v[58:61], v[82:85], a[28:31]
	ds_read_b128 v[34:37], v164 offset:2048
	v_mfma_f32_16x16x32_f16 a[60:63], v[58:61], v[86:89], a[60:63]
	ds_read_b128 v[30:33], v164 offset:3072
	v_mfma_f32_16x16x32_f16 a[8:11], v[54:57], v[82:85], a[8:11]
	ds_read_b128 v[26:29], v164 offset:4096
	v_mfma_f32_16x16x32_f16 a[20:23], v[54:57], v[86:89], a[20:23]
	ds_read_b128 v[22:25], v164 offset:5120
	v_mfma_f32_16x16x32_f16 a[24:27], v[46:49], v[82:85], a[24:27]
	ds_read_b128 v[10:13], v164 offset:6144
	v_mfma_f32_16x16x32_f16 a[36:39], v[46:49], v[86:89], a[36:39]
	ds_read_b128 v[6:9], v164 offset:7168
	v_mfma_f32_16x16x32_f16 a[44:47], v[50:53], v[82:85], a[44:47]
	ds_read_b128 v[2:5], v164 offset:8192
	v_mfma_f32_16x16x32_f16 a[64:67], v[50:53], v[86:89], a[64:67]
	v_mfma_f32_16x16x32_f16 a[32:35], v[62:65], v[82:85], a[32:35]
	v_mfma_f32_16x16x32_f16 a[40:43], v[62:65], v[86:89], a[40:43]
	v_mfma_f32_16x16x32_f16 a[48:51], v[74:77], v[82:85], a[48:51]
	v_mfma_f32_16x16x32_f16 a[52:55], v[74:77], v[86:89], a[52:55]
	v_mfma_f32_16x16x32_f16 a[56:59], v[78:81], v[82:85], a[56:59]
	v_mfma_f32_16x16x32_f16 a[68:71], v[78:81], v[86:89], a[68:71]
	s_waitcnt lgkmcnt(8)
	v_mfma_f32_16x16x32_f16 a[0:3], v[42:45], v[14:17], a[0:3]
	ds_read_b128 v[82:85], v161
	v_mfma_f32_16x16x32_f16 a[4:7], v[42:45], v[18:21], a[4:7]
	ds_read_b128 v[86:89], v163
	s_waitcnt lgkmcnt(9)
	v_mfma_f32_16x16x32_f16 a[12:15], v[38:41], v[14:17], a[12:15]
	ds_read_b128 v[70:73], v164 offset:9216
	v_mfma_f32_16x16x32_f16 a[16:19], v[38:41], v[18:21], a[16:19]
	ds_read_b128 v[66:69], v164 offset:10240
	s_waitcnt lgkmcnt(10)
	v_mfma_f32_16x16x32_f16 a[28:31], v[34:37], v[14:17], a[28:31]
	ds_read_b128 v[58:61], v164 offset:11264
	v_mfma_f32_16x16x32_f16 a[60:63], v[34:37], v[18:21], a[60:63]
	ds_read_b128 v[54:57], v164 offset:12288
	s_waitcnt lgkmcnt(11)
	v_mfma_f32_16x16x32_f16 a[8:11], v[30:33], v[14:17], a[8:11]
	ds_read_b128 v[46:49], v164 offset:13312
	v_mfma_f32_16x16x32_f16 a[20:23], v[30:33], v[18:21], a[20:23]
	ds_read_b128 v[50:53], v164 offset:14336
	s_waitcnt lgkmcnt(12)
	v_mfma_f32_16x16x32_f16 a[24:27], v[26:29], v[14:17], a[24:27]
	ds_read_b128 v[62:65], v164 offset:15360
	v_mfma_f32_16x16x32_f16 a[36:39], v[26:29], v[18:21], a[36:39]
	ds_read_b128 v[74:77], v164 offset:16384
	s_waitcnt lgkmcnt(13)
	v_mfma_f32_16x16x32_f16 a[44:47], v[22:25], v[14:17], a[44:47]
	ds_read_b128 v[78:81], v164 offset:17408
	v_mfma_f32_16x16x32_f16 a[64:67], v[22:25], v[18:21], a[64:67]
	s_waitcnt lgkmcnt(13)
	v_mfma_f32_16x16x32_f16 a[32:35], v[10:13], v[14:17], a[32:35]
	v_mfma_f32_16x16x32_f16 a[40:43], v[10:13], v[18:21], a[40:43]
	s_waitcnt lgkmcnt(12)
	v_mfma_f32_16x16x32_f16 a[48:51], v[6:9], v[14:17], a[48:51]
	v_mfma_f32_16x16x32_f16 a[52:55], v[6:9], v[18:21], a[52:55]
	s_waitcnt lgkmcnt(11)
	v_mfma_f32_16x16x32_f16 a[56:59], v[2:5], v[14:17], a[56:59]
	v_mfma_f32_16x16x32_f16 a[68:71], v[2:5], v[18:21], a[68:71]
	s_waitcnt lgkmcnt(8)
	v_mfma_f32_16x16x32_f16 a[0:3], v[70:73], v[82:85], a[0:3]
	v_mfma_f32_16x16x32_f16 a[4:7], v[70:73], v[86:89], a[4:7]
	s_waitcnt lgkmcnt(9)
	v_mfma_f32_16x16x32_f16 a[12:15], v[66:69], v[82:85], a[12:15]
	v_mfma_f32_16x16x32_f16 a[16:19], v[66:69], v[86:89], a[16:19]
	s_waitcnt lgkmcnt(10)
	v_mfma_f32_16x16x32_f16 a[28:31], v[58:61], v[82:85], a[28:31]
	v_mfma_f32_16x16x32_f16 a[60:63], v[58:61], v[86:89], a[60:63]
	s_waitcnt lgkmcnt(11)
	v_mfma_f32_16x16x32_f16 a[8:11], v[54:57], v[82:85], a[8:11]
	v_mfma_f32_16x16x32_f16 a[20:23], v[54:57], v[86:89], a[20:23]
	s_waitcnt lgkmcnt(12)
	v_mfma_f32_16x16x32_f16 a[24:27], v[46:49], v[82:85], a[24:27]
	v_mfma_f32_16x16x32_f16 a[36:39], v[46:49], v[86:89], a[36:39]
	s_waitcnt lgkmcnt(13)
	v_mfma_f32_16x16x32_f16 a[44:47], v[50:53], v[82:85], a[44:47]
	v_mfma_f32_16x16x32_f16 a[64:67], v[50:53], v[86:89], a[64:67]
	s_waitcnt lgkmcnt(13)
	v_mfma_f32_16x16x32_f16 a[32:35], v[62:65], v[82:85], a[32:35]
	v_mfma_f32_16x16x32_f16 a[40:43], v[62:65], v[86:89], a[40:43]
	s_waitcnt lgkmcnt(12)
	v_mfma_f32_16x16x32_f16 a[48:51], v[74:77], v[82:85], a[48:51]
	v_mfma_f32_16x16x32_f16 a[52:55], v[74:77], v[86:89], a[52:55]
	s_waitcnt lgkmcnt(11)
	v_mfma_f32_16x16x32_f16 a[56:59], v[78:81], v[82:85], a[56:59]
	v_mfma_f32_16x16x32_f16 a[68:71], v[78:81], v[86:89], a[68:71]
	s_waitcnt lgkmcnt(0)
	s_setprio 0
